# stack7_nt + non-temporal hint on the fp8 weight stores of the P2 conversion (stream and dedicated pass)
# speedup vs baseline: 1.0153x; 1.0153x over previous
; #define G8_STAGE(bufoff, gbase, v0, v1) do { unsigned x0_ = (v0), x1_ = (v1); asm volatile("" : "+v"(x0_), "+v"(x1_));     \
;         __builtin_amdgcn_global_load_lds((const unsigned*)((gbase) + x0_), (LAS unsigned*)(lds + (bufoff) + ldsw), 16, 0, 0); \
;         __builtin_amdgcn_global_load_lds((const unsigned*)((gbase) + x1_), (LAS unsigned*)(lds + (bufoff) + ldsw + 8192), 16, 0, 0); } while (0)
; #define G8_LDA(dst, b, h) do { _Pragma("unroll") for (int m = 0; m < 4; ++m) _Pragma("unroll") for (int k = 0; k < 2; ++k) dst[m][k] = *(const LAS bf16x8*)(lds + G8_SA(b, h) + aoff + m * 2048 + k * 1024); } while (0)
; #define G8_LDB(dst, b, h) do { _Pragma("unroll") for (int n = 0; n < 2; ++n) _Pragma("unroll") for (int k = 0; k < 2; ++k) dst[n][k] = *(const LAS bf16x8*)(lds + G8_SB(b, h) + boff + n * 2048 + k * 1024); } while (0)
; #define G8_WAIT_L(n) asm volatile("s_waitcnt lgkmcnt(" #n ")" ::: "memory")
; #define G8_BAR __builtin_amdgcn_s_barrier()
; #define G8_SCHED __builtin_amdgcn_sched_barrier(0)
;     ...
;             G8_CONV_READ; G8_SCHED;
;             G8_LDB(B0, 0, 0); G8_SCHED; G8_LDA(At, 0, 0); G8_STAGE(G8_SA(1, 1), a1, cv[1][0], cv[1][1]);
;             G8_WAIT_L(8); G8_BAR; G8_WAIT_L(0); if (do0) G8_MMA(0, 0, At, B0); G8_CONV_CVT; G8_BAR; G8_SCHED;
;             G8_LDB(B1, 0, 1); G8_STAGE(G8_SB(0, 0), b2, voffB[0], voffB[1]);
;             G8_BAR; G8_CONV_ISSUE;
.LBB0_234:
	s_add_u32 s4, s0, 0x80
	s_addc_u32 s5, s1, 0
	s_add_u32 s42, s0, 0x100
	s_addc_u32 s43, s1, 0
	s_add_u32 s49, s6, 0x10000
	s_addc_u32 s62, s7, 0
	s_cmp_eq_u32 s61, 28
	s_cselect_b32 s47, s69, s43
	s_cselect_b32 s46, s76, s42
	s_cselect_b32 s43, s57, s62
	s_cselect_b32 s42, s60, s49
	s_mov_b32 s49, 0
	s_nop 0
	v_mbcnt_lo_u32_b32 v130, -1, s49
	v_mbcnt_hi_u32_b32 v130, -1, v130
	v_and_b32_e32 v131, 15, v130
	v_lshrrev_b32_e32 v130, 2, v130
	v_mul_u32_u24_e32 v131, 0x410, v131
	v_and_b32_e32 v130, 0x3ffffffc, v130
	v_add3_u32 v130, s96, v131, v130
	ds_read2_b32 v[146:147], v130 offset1:32
	ds_read2_b32 v[148:149], v130 offset0:64 offset1:96
	ds_read2_b32 v[212:213], v130 offset0:128 offset1:160
	ds_read2_b32 v[214:215], v130 offset0:192 offset1:224
	s_add_i32 s49, 0, 0x10000
	v_add_u32_e32 v142, s49, v209
	ds_read_b128 v[130:133], v142
	ds_read_b128 v[134:137], v142 offset:1024
	ds_read_b128 v[138:141], v142 offset:2048
	ds_read_b128 v[142:145], v142 offset:3072
	v_mov_b32_e32 v150, v204
	v_mov_b32_e32 v151, v203
	s_add_i32 m0, s78, 0xc000
	ds_read_b128 v[186:189], v210
	ds_read_b128 v[190:193], v210 offset:1024
	ds_read_b128 v[178:181], v210 offset:2048
	ds_read_b128 v[182:185], v210 offset:3072
	ds_read_b128 v[170:173], v210 offset:4096
	ds_read_b128 v[174:177], v210 offset:5120
	ds_read_b128 v[162:165], v210 offset:6144
	ds_read_b128 v[166:169], v210 offset:7168
	s_nop 0
	global_load_lds_dwordx4 v151, s[4:5]
	s_add_i32 m0, s78, 0xe000
	s_nop 0
	global_load_lds_dwordx4 v150, s[4:5]
	s_waitcnt lgkmcnt(8)
	s_barrier
	s_waitcnt lgkmcnt(0)
	s_setprio 1
	s_waitcnt lgkmcnt(0)
	v_mfma_f32_16x16x32_bf16 v[126:129], v[130:133], v[186:189], v[126:129]
	v_mfma_f32_16x16x32_bf16 v[122:125], v[138:141], v[186:189], v[122:125]
	v_mfma_f32_16x16x32_bf16 v[118:121], v[130:133], v[178:181], v[118:121]
	v_mfma_f32_16x16x32_bf16 v[114:117], v[138:141], v[178:181], v[114:117]
	v_mfma_f32_16x16x32_bf16 v[110:113], v[130:133], v[170:173], v[110:113]
	v_mfma_f32_16x16x32_bf16 v[106:109], v[138:141], v[170:173], v[106:109]
	v_mfma_f32_16x16x32_bf16 v[102:105], v[130:133], v[162:165], v[102:105]
	v_mfma_f32_16x16x32_bf16 v[98:101], v[138:141], v[162:165], v[98:101]
	v_mfma_f32_16x16x32_bf16 v[126:129], v[134:137], v[190:193], v[126:129]
	v_mfma_f32_16x16x32_bf16 v[122:125], v[142:145], v[190:193], v[122:125]
	v_mfma_f32_16x16x32_bf16 v[118:121], v[134:137], v[182:185], v[118:121]
	v_mfma_f32_16x16x32_bf16 v[114:117], v[142:145], v[182:185], v[114:117]
	v_mfma_f32_16x16x32_bf16 v[110:113], v[134:137], v[174:177], v[110:113]
	v_mfma_f32_16x16x32_bf16 v[106:109], v[142:145], v[174:177], v[106:109]
	v_mfma_f32_16x16x32_bf16 v[102:105], v[134:137], v[166:169], v[102:105]
	v_mfma_f32_16x16x32_bf16 v[98:101], v[142:145], v[166:169], v[98:101]
	s_setprio 0
	v_mul_f32_e32 v146, s59, v146
	v_mul_f32_e32 v147, s59, v147
	v_mov_b32_e32 v216, 0
	v_cvt_pk_fp8_f32 v216, v146, v147
	v_mul_f32_e32 v146, s59, v148
	v_mul_f32_e32 v147, s59, v149
	v_mul_f32_e32 v194, s59, v213
	v_cvt_pk_fp8_f32 v216, v146, v147 op_sel:[0,0,1]
	v_mul_f32_e32 v213, s59, v215
	s_barrier
	v_mul_f32_e32 v212, s59, v212
	v_mov_b32_e32 v217, 0
	v_cvt_pk_fp8_f32 v217, v212, v194
	v_mul_f32_e32 v194, s59, v214
	s_add_i32 s4, s49, s77
	v_mov_b32_e32 v212, v198
	v_cvt_pk_fp8_f32 v217, v194, v213 op_sel:[0,0,1]
	v_mov_b32_e32 v194, v1
	s_mov_b32 m0, s4
	ds_read_b128 v[146:149], v211
	ds_read_b128 v[150:153], v211 offset:1024
	ds_read_b128 v[154:157], v211 offset:2048
	ds_read_b128 v[158:161], v211 offset:3072
	s_min_i32 s62, s68, s52
	global_load_lds_dwordx4 v194, s[42:43]
	s_add_i32 m0, s4, 0x2000
	s_mov_b32 s4, 0
	global_load_lds_dwordx4 v212, s[42:43]
	s_barrier
	s_ashr_i32 s64, s62, 2
	v_mbcnt_lo_u32_b32 v194, -1, s4
	v_mbcnt_hi_u32_b32 v194, -1, v194
	v_lshlrev_b32_e32 v212, 3, v194
	v_and_b32_e32 v213, 0xffffff80, v212
	v_add_u32_e32 v213, s97, v213
	s_movk_i32 s4, 0x78
	v_and_or_b32 v212, v212, s4, v213
	s_cmp_eq_u32 s64, s48
	global_store_dwordx2 v212, v[216:217], s[40:41] nt
	s_cbranch_scc1 .LBB0_241
	s_mul_i32 s41, s64, s33
	s_add_i32 s41, s41, s2
	s_cmpk_gt_i32 s41, 0x1fff
	s_mov_b64 s[48:49], -1
	s_cbranch_scc0 .LBB0_237
	s_add_i32 s4, s41, 0xffffe000
	s_lshr_b32 s14, s4, 7
	s_lshl_b64 s[4:5], s[14:15], 23
	s_add_u32 s28, s18, s4
	s_addc_u32 s29, s19, s5
	s_lshl_b64 s[4:5], s[14:15], 21
	s_add_u32 s30, s53, s4
	s_addc_u32 s31, s54, s5
	s_lshl_b32 s4, s41, 3
	s_and_b32 s67, s4, 0x380
	s_lshl_b32 s4, s41, 7
	s_and_b32 s40, s4, 0x780
	s_mov_b64 s[48:49], 0

; #define LAS __attribute__((address_space(3)))
; __device__ __forceinline__ void cvt8_store(const LAS unsigned* tile, const Cvt8Unit& u, int tid) {
;     const int nl = tid >> 2, q = tid & 3;
;     u32x4 w0, w1;
;     w0.x = tile[(8 * q + 0) * 132 + nl]; w0.y = tile[(8 * q + 1) * 132 + nl]; w0.z = tile[(8 * q + 2) * 132 + nl]; w0.w = tile[(8 * q + 3) * 132 + nl];
;     w1.x = tile[(8 * q + 4) * 132 + nl]; w1.y = tile[(8 * q + 5) * 132 + nl]; w1.z = tile[(8 * q + 6) * 132 + nl]; w1.w = tile[(8 * q + 7) * 132 + nl];
;     const int n = u.n0 + nl;
;     int np = n;
;     if (u.nmode == 1 || u.nmode == 2) np = (n >> 7) * 256 + (n & 127) + (u.nmode == 2 ? 128 : 0);
;     unsigned char* d = u.dst + (size_t)(np >> 8) * ((size_t)u.Kd * 256) + (size_t)(u.k0 >> 7) * 32768 + (np & 255) * 128 + q * 32;
;     *(u32x4*)d = w0; *(u32x4*)(d + 16) = w1;
; }
.LBB0_318:
	s_add_i32 s29, s43, -1
	v_add_u32_e32 v42, s68, v134
	s_cmp_lt_u32 s29, 2
	s_cselect_b64 vcc, -1, 0
	v_lshlrev_b32_e32 v43, 1, v42
	s_cmp_eq_u32 s43, 2
	v_and_b32_e32 v43, 0xffffff00, v43
	v_and_b32_e32 v44, 0x7f, v42
	s_cselect_b32 s29, 0x80, 0
	v_or3_b32 v43, v44, s29, v43
	v_cndmask_b32_e32 v44, v42, v43, vcc
	v_ashrrev_i32_e32 v45, 8, v44
	v_ashrrev_i32_e32 v42, 31, v45
	s_lshl_b32 s29, s42, 8
	v_mul_lo_u32 v46, s29, v42
	v_mov_b64_e32 v[42:43], s[40:41]
	s_ashr_i32 s43, s42, 31
	v_mad_u64_u32 v[42:43], s[40:41], s29, v45, v[42:43]
	v_add_u32_e32 v32, 0x400, v138
	v_add_u32_e32 v38, 0x800, v138
	v_add_u32_e32 v40, 0xc00, v138
	s_lshr_b64 s[42:43], s[42:43], 24
	s_ashr_i32 s40, s66, 7
	s_waitcnt lgkmcnt(0)
	s_barrier
	ds_read2_b32 v[30:31], v138 offset1:132
	ds_read2_b32 v[32:33], v32 offset0:8 offset1:140
	ds_read2_b32 v[38:39], v38 offset0:16 offset1:148
	ds_read2_b32 v[40:41], v40 offset0:24 offset1:156
	v_mul_i32_i24_e32 v47, s42, v45
	s_ashr_i32 s41, s40, 31
	v_add3_u32 v43, v47, v43, v46
	s_lshl_b64 s[40:41], s[40:41], 15
	v_lshlrev_b32_e32 v44, 7, v44
	v_lshl_add_u64 v[42:43], v[42:43], 0, s[40:41]
	v_and_b32_e32 v194, 0x7f80, v44
	v_lshl_add_u64 v[42:43], v[42:43], 0, v[194:195]
	v_lshl_add_u64 v[42:43], v[42:43], 0, v[132:133]
	s_and_b64 vcc, exec, s[6:7]
	s_waitcnt lgkmcnt(2)
	global_store_dwordx4 v[42:43], v[30:33], off nt
	s_waitcnt lgkmcnt(0)
	global_store_dwordx4 v[42:43], v[38:41], off offset:16 nt
	s_cbranch_vccnz .LBB0_320
	s_add_i32 s6, s37, -1
	v_add_u32_e32 v42, s63, v134
	s_cmp_lt_u32 s6, 2
	s_cselect_b64 vcc, -1, 0
	v_lshlrev_b32_e32 v43, 1, v42
	s_cmp_eq_u32 s37, 2
	v_and_b32_e32 v43, 0xffffff00, v43
	v_and_b32_e32 v44, 0x7f, v42
	s_cselect_b32 s6, 0x80, 0
	v_or3_b32 v43, v44, s6, v43
	v_cndmask_b32_e32 v44, v42, v43, vcc
	v_ashrrev_i32_e32 v45, 8, v44
	v_ashrrev_i32_e32 v42, 31, v45
	s_ashr_i32 s37, s36, 31
	s_lshl_b32 s29, s36, 8
	v_mul_lo_u32 v46, s29, v42
	s_lshr_b64 s[6:7], s[36:37], 24
	v_mov_b64_e32 v[42:43], s[34:35]
	v_mul_i32_i24_e32 v47, s6, v45
	v_mad_u64_u32 v[42:43], s[6:7], s29, v45, v[42:43]
	v_add_u32_e32 v30, 0x4200, v138
	v_add_u32_e32 v32, 0x4600, v138
	s_ashr_i32 s6, s61, 7
	ds_read2_b32 v[30:31], v30 offset1:132
	ds_read2_b32 v[32:33], v32 offset0:8 offset1:140
	v_add_u32_e32 v38, 0x4a00, v138
	v_add_u32_e32 v40, 0x4e00, v138
	s_ashr_i32 s7, s6, 31
	ds_read2_b32 v[38:39], v38 offset0:16 offset1:148
	ds_read2_b32 v[40:41], v40 offset0:24 offset1:156
	v_add3_u32 v43, v47, v43, v46
	s_lshl_b64 s[6:7], s[6:7], 15
	v_lshlrev_b32_e32 v44, 7, v44
	v_lshl_add_u64 v[42:43], v[42:43], 0, s[6:7]
	v_and_b32_e32 v194, 0x7f80, v44
	v_lshl_add_u64 v[42:43], v[42:43], 0, v[194:195]
	v_lshl_add_u64 v[42:43], v[42:43], 0, v[132:133]
	s_waitcnt lgkmcnt(2)
	global_store_dwordx4 v[42:43], v[30:33], off nt
	s_waitcnt lgkmcnt(0)
	global_store_dwordx4 v[42:43], v[38:41], off offset:16 nt
